# scanner waves raised to priority 2 so their load issue is not delayed by the gatherer wave on the same SIMD
# speedup vs baseline: 1.0019x; 1.0015x over previous
.LBB1_217:
	s_andn2_saveexec_b64 s[0:1], s[30:31]
	s_cbranch_execz .LBB1_384
	s_setprio 2
	v_readfirstlane_b32 s34, v1
	v_readfirstlane_b32 s37, v82
	v_readfirstlane_b32 s36, v84
	v_and_b32_e32 v3, 63, v0
	v_lshlrev_b32_e32 v2, 4, v3
	s_cmp_lt_i32 s36, 0
	s_cbranch_scc1 .LBB1_384
	s_waitcnt lgkmcnt(0)
	s_and_b32 s29, s29, 0xffff
	s_mov_b32 s30, 0x17d78400
	s_mov_b32 s31, 0x20000
	s_mov_b32 s35, 0
	s_movk_i32 s7, 0x80
	s_mov_b32 s9, 0x7fffffff
	s_lshl_b32 s44, s34, 12
	s_add_u32 s44, s44, 0x4000
	s_lshl_b32 s45, s34, 10
	s_add_u32 s45, s45, 0x8000
	s_lshl_b32 s46, s34, 3
	s_add_u32 s46, s46, 0x9000
	s_and_b32 s47, s37, 1
	s_lshl_b32 s47, s47, 2
	s_mul_i32 s38, s37, 0x9c40
	s_lshl_b32 s40, s47, 4
	s_sub_u32 s38, s38, s40
	v_max_u32_e32 v12, s47, v3
	v_lshlrev_b32_e32 v12, 4, v12
